# prep: x->f16 conversion blocks paired (even block converts 2 rows-chunks per thread with 4 loads in flight, odd block exits)
# baseline (speedup 1.0000x reference)
.LBB0_9:
	s_andn2_saveexec_b64 s[4:5], s[6:7]
	s_cbranch_execz .LBB0_11
	s_sub_i32 s12, s2, 64
	s_cmpk_lt_u32 s12, 0x61a
	s_cbranch_scc0 .Lprep_single
	s_bitcmp1_b32 s12, 0
	s_cbranch_scc1 .LBB0_11
	s_load_dwordx4 s[8:11], s[0:1], 0x0
	v_ashrrev_i32_e32 v4, 4, v2
	v_ashrrev_i32_e32 v5, 31, v4
	v_lshlrev_b32_e32 v1, 4, v0
	v_lshlrev_b64 v[4:5], 9, v[4:5]
	s_waitcnt lgkmcnt(0)
	v_lshl_add_u64 v[4:5], s[8:9], 0, v[4:5]
	v_and_b32_e32 v6, 0xf0, v1
	v_mov_b32_e32 v7, 0
	v_lshl_add_u64 v[12:13], v[4:5], 0, v[6:7]
	global_load_dwordx4 v[4:7], v[12:13], off offset:256 nt
	global_load_dwordx4 v[8:11], v[12:13], off nt
	s_mov_b64 s[12:13], 0x8000
	v_lshl_add_u64 v[14:15], v[12:13], 0, s[12:13]
	global_load_dwordx4 v[16:19], v[14:15], off offset:256 nt
	global_load_dwordx4 v[20:23], v[14:15], off nt
	v_ashrrev_i32_e32 v3, 31, v2
	v_lshl_add_u64 v[2:3], v[2:3], 4, s[10:11]
	s_mov_b64 s[12:13], 0x4000
	v_lshl_add_u64 v[24:25], v[2:3], 0, s[12:13]
	s_waitcnt vmcnt(3)
	v_cvt_pk_f16_f32 v7, v6, v7
	v_cvt_pk_f16_f32 v6, v4, v5
	s_waitcnt vmcnt(2)
	v_cvt_pk_f16_f32 v5, v10, v11
	v_cvt_pk_f16_f32 v4, v8, v9
	global_store_dwordx4 v[2:3], v[4:7], off sc1
	s_waitcnt vmcnt(2)
	v_cvt_pk_f16_f32 v19, v18, v19
	v_cvt_pk_f16_f32 v18, v16, v17
	s_waitcnt vmcnt(1)
	v_cvt_pk_f16_f32 v17, v22, v23
	v_cvt_pk_f16_f32 v16, v20, v21
	global_store_dwordx4 v[24:25], v[16:19], off sc1
	s_nop 1
	s_branch .LBB0_11
.Lprep_single:
	s_load_dwordx4 s[8:11], s[0:1], 0x0
	v_ashrrev_i32_e32 v4, 4, v2
	v_ashrrev_i32_e32 v5, 31, v4
	v_lshlrev_b32_e32 v1, 4, v0
	v_lshlrev_b64 v[4:5], 9, v[4:5]
	s_waitcnt lgkmcnt(0)
	v_lshl_add_u64 v[4:5], s[8:9], 0, v[4:5]
	v_and_b32_e32 v6, 0xf0, v1
	v_mov_b32_e32 v7, 0
	v_lshl_add_u64 v[12:13], v[4:5], 0, v[6:7]
	global_load_dwordx4 v[4:7], v[12:13], off offset:256 nt
	global_load_dwordx4 v[8:11], v[12:13], off nt
	v_ashrrev_i32_e32 v3, 31, v2
	v_lshl_add_u64 v[2:3], v[2:3], 4, s[10:11]
	s_waitcnt vmcnt(1)
	v_cvt_pk_f16_f32 v7, v6, v7
	v_cvt_pk_f16_f32 v6, v4, v5
	s_waitcnt vmcnt(0)
	v_cvt_pk_f16_f32 v5, v10, v11
	v_cvt_pk_f16_f32 v4, v8, v9
	global_store_dwordx4 v[2:3], v[4:7], off sc1
	s_nop 1

	.amdhsa_kernel _Z17prep_count_kernelPKfPDv8_DF16_S0_S0_S2_PKiPiP15HIP_vector_typeIfLj4EE
		.amdhsa_group_segment_fixed_size 6400
		.amdhsa_private_segment_fixed_size 0
		.amdhsa_kernarg_size 64
		.amdhsa_user_sgpr_count 2
		.amdhsa_user_sgpr_dispatch_ptr 0
		.amdhsa_user_sgpr_queue_ptr 0
		.amdhsa_user_sgpr_kernarg_segment_ptr 1
		.amdhsa_user_sgpr_dispatch_id 0
		.amdhsa_user_sgpr_kernarg_preload_length 0
		.amdhsa_user_sgpr_kernarg_preload_offset 0
		.amdhsa_user_sgpr_private_segment_size 0
		.amdhsa_uses_dynamic_stack 0
		.amdhsa_enable_private_segment 0
		.amdhsa_system_sgpr_workgroup_id_x 1
		.amdhsa_system_sgpr_workgroup_id_y 0
		.amdhsa_system_sgpr_workgroup_id_z 0
		.amdhsa_system_sgpr_workgroup_info 0
		.amdhsa_system_vgpr_workitem_id 0
		.amdhsa_next_free_vgpr 26
		.amdhsa_next_free_sgpr 16
		.amdhsa_accum_offset 28
		.amdhsa_reserve_vcc 1
		.amdhsa_float_round_mode_32 0
		.amdhsa_float_round_mode_16_64 0
		.amdhsa_float_denorm_mode_32 3
		.amdhsa_float_denorm_mode_16_64 3
		.amdhsa_dx10_clamp 1
		.amdhsa_ieee_mode 1
		.amdhsa_fp16_overflow 0
		.amdhsa_tg_split 0
		.amdhsa_exception_fp_ieee_invalid_op 0
		.amdhsa_exception_fp_denorm_src 0
		.amdhsa_exception_fp_ieee_div_zero 0
		.amdhsa_exception_fp_ieee_overflow 0
		.amdhsa_exception_fp_ieee_underflow 0
		.amdhsa_exception_fp_ieee_inexact 0
		.amdhsa_exception_int_div_zero 0
	.end_amdhsa_kernel

amdhsa.kernels:
  - .agpr_count:     0
    .args:
      - .actual_access:  read_only
        .address_space:  global
        .offset:         0
        .size:           8
        .value_kind:     global_buffer
      - .address_space:  global
        .offset:         8
        .size:           8
        .value_kind:     global_buffer
      - .actual_access:  read_only
        .address_space:  global
        .offset:         16
        .size:           8
        .value_kind:     global_buffer
      - .actual_access:  read_only
        .address_space:  global
        .offset:         24
        .size:           8
        .value_kind:     global_buffer
      - .actual_access:  write_only
        .address_space:  global
        .offset:         32
        .size:           8
        .value_kind:     global_buffer
      - .actual_access:  read_only
        .address_space:  global
        .offset:         40
        .size:           8
        .value_kind:     global_buffer
      - .actual_access:  write_only
        .address_space:  global
        .offset:         48
        .size:           8
        .value_kind:     global_buffer
      - .actual_access:  write_only
        .address_space:  global
        .offset:         56
        .size:           8
        .value_kind:     global_buffer
    .group_segment_fixed_size: 6400
    .kernarg_segment_align: 8
    .kernarg_segment_size: 64
    .language:       OpenCL C
    .language_version:
      - 2
      - 0
    .max_flat_workgroup_size: 1024
    .name:           _Z17prep_count_kernelPKfPDv8_DF16_S0_S0_S2_PKiPiP15HIP_vector_typeIfLj4EE
    .private_segment_fixed_size: 0
    .sgpr_count:     22
    .sgpr_spill_count: 0
    .symbol:         _Z17prep_count_kernelPKfPDv8_DF16_S0_S0_S2_PKiPiP15HIP_vector_typeIfLj4EE.kd
    .uniform_work_group_size: 1
    .uses_dynamic_stack: false
    .vgpr_count:     26
    .vgpr_spill_count: 0
    .wavefront_size: 64
  - .agpr_count:     0
    .args:
      - .actual_access:  read_only
        .address_space:  global
        .offset:         0
        .size:           8
        .value_kind:     global_buffer
      - .actual_access:  read_only
        .address_space:  global
        .offset:         8
        .size:           8
        .value_kind:     global_buffer
      - .actual_access:  read_only
        .address_space:  global
        .offset:         16
        .size:           8
        .value_kind:     global_buffer
      - .actual_access:  write_only
        .address_space:  global
        .offset:         24
        .size:           8
        .value_kind:     global_buffer
      - .actual_access:  write_only
        .address_space:  global
        .offset:         32
        .size:           8
        .value_kind:     global_buffer
    .group_segment_fixed_size: 124704
    .kernarg_segment_align: 8
    .kernarg_segment_size: 40
    .language:       OpenCL C
    .language_version:
      - 2
      - 0
    .max_flat_workgroup_size: 1024
    .name:           _Z14scatter_kernelPKiS0_S0_PiP15HIP_vector_typeIiLj2EE
    .private_segment_fixed_size: 0
    .sgpr_count:     55
    .sgpr_spill_count: 0
    .symbol:         _Z14scatter_kernelPKiS0_S0_PiP15HIP_vector_typeIiLj2EE.kd
    .uniform_work_group_size: 1
    .uses_dynamic_stack: false
    .vgpr_count:     128
    .vgpr_spill_count: 0
    .wavefront_size: 64
  - .agpr_count:     0
    .args:
      - .actual_access:  read_only
        .address_space:  global
        .offset:         0
        .size:           8
        .value_kind:     global_buffer
      - .address_space:  global
        .offset:         8
        .size:           8
        .value_kind:     global_buffer
      - .address_space:  global
        .offset:         16
        .size:           8
        .value_kind:     global_buffer
      - .actual_access:  read_only
        .address_space:  global
        .offset:         24
        .size:           8
        .value_kind:     global_buffer
      - .actual_access:  read_only
        .address_space:  global
        .offset:         32
        .size:           8
        .value_kind:     global_buffer
      - .actual_access:  read_only
        .address_space:  global
        .offset:         40
        .size:           8
        .value_kind:     global_buffer
      - .offset:         48
        .size:           4
        .value_kind:     hidden_block_count_x
      - .offset:         52
        .size:           4
        .value_kind:     hidden_block_count_y
      - .offset:         56
        .size:           4
        .value_kind:     hidden_block_count_z
      - .offset:         60
        .size:           2
        .value_kind:     hidden_group_size_x
      - .offset:         62
        .size:           2
        .value_kind:     hidden_group_size_y
      - .offset:         64
        .size:           2
        .value_kind:     hidden_group_size_z
      - .offset:         66
        .size:           2
        .value_kind:     hidden_remainder_x
      - .offset:         68
        .size:           2
        .value_kind:     hidden_remainder_y
      - .offset:         70
        .size:           2
        .value_kind:     hidden_remainder_z
      - .offset:         88
        .size:           8
        .value_kind:     hidden_global_offset_x
      - .offset:         96
        .size:           8
        .value_kind:     hidden_global_offset_y
      - .offset:         104
        .size:           8
        .value_kind:     hidden_global_offset_z
      - .offset:         112
        .size:           2
        .value_kind:     hidden_grid_dims
    .group_segment_fixed_size: 1024
    .kernarg_segment_align: 8
    .kernarg_segment_size: 304
    .language:       OpenCL C
    .language_version:
      - 2
      - 0
    .max_flat_workgroup_size: 256
    .name:           _Z9bn_kernelPKDv8_DF16_S1_PS_PKfS4_S4_
    .private_segment_fixed_size: 0
    .sgpr_count:     20
    .sgpr_spill_count: 0
    .symbol:         _Z9bn_kernelPKDv8_DF16_S1_PS_PKfS4_S4_.kd
    .uniform_work_group_size: 1
    .uses_dynamic_stack: false
    .vgpr_count:     64
    .vgpr_spill_count: 0
    .wavefront_size: 64
  - .agpr_count:     0
    .args:
      - .actual_access:  read_only
        .address_space:  global
        .offset:         0
        .size:           8
        .value_kind:     global_buffer
      - .actual_access:  read_only
        .address_space:  global
        .offset:         8
        .size:           8
        .value_kind:     global_buffer
      - .actual_access:  read_only
        .address_space:  global
        .offset:         16
        .size:           8
        .value_kind:     global_buffer
      - .actual_access:  read_only
        .address_space:  global
        .offset:         24
        .size:           8
        .value_kind:     global_buffer
      - .actual_access:  read_only
        .address_space:  global
        .offset:         32
        .size:           8
        .value_kind:     global_buffer
      - .actual_access:  read_only
        .address_space:  global
        .offset:         40
        .size:           8
        .value_kind:     global_buffer
      - .actual_access:  read_only
        .address_space:  global
        .offset:         48
        .size:           8
        .value_kind:     global_buffer
      - .actual_access:  write_only
        .address_space:  global
        .offset:         56
        .size:           8
        .value_kind:     global_buffer
      - .offset:         64
        .size:           4
        .value_kind:     hidden_block_count_x
      - .offset:         68
        .size:           4
        .value_kind:     hidden_block_count_y
      - .offset:         72
        .size:           4
        .value_kind:     hidden_block_count_z
      - .offset:         76
        .size:           2
        .value_kind:     hidden_group_size_x
      - .offset:         78
        .size:           2
        .value_kind:     hidden_group_size_y
      - .offset:         80
        .size:           2
        .value_kind:     hidden_group_size_z
      - .offset:         82
        .size:           2
        .value_kind:     hidden_remainder_x
      - .offset:         84
        .size:           2
        .value_kind:     hidden_remainder_y
      - .offset:         86
        .size:           2
        .value_kind:     hidden_remainder_z
      - .offset:         104
        .size:           8
        .value_kind:     hidden_global_offset_x
      - .offset:         112
        .size:           8
        .value_kind:     hidden_global_offset_y
      - .offset:         120
        .size:           8
        .value_kind:     hidden_global_offset_z
      - .offset:         128
        .size:           2
        .value_kind:     hidden_grid_dims
    .group_segment_fixed_size: 34816
    .kernarg_segment_align: 8
    .kernarg_segment_size: 320
    .language:       OpenCL C
    .language_version:
      - 2
      - 0
    .max_flat_workgroup_size: 512
    .name:           _Z12final_kernelPKDv8_DF16_S1_PKfS3_S3_S1_S3_Pf
    .private_segment_fixed_size: 0
    .sgpr_count:     34
    .sgpr_spill_count: 0
    .symbol:         _Z12final_kernelPKDv8_DF16_S1_PKfS3_S3_S1_S3_Pf.kd
    .uniform_work_group_size: 1
    .uses_dynamic_stack: false
    .vgpr_count:     60
    .vgpr_spill_count: 0
    .wavefront_size: 64
  - .agpr_count:     0
    .args:
      - .actual_access:  read_only
        .address_space:  global
        .offset:         0
        .size:           8
        .value_kind:     global_buffer
      - .actual_access:  read_only
        .address_space:  global
        .offset:         8
        .size:           8
        .value_kind:     global_buffer
      - .address_space:  global
        .offset:         16
        .size:           8
        .value_kind:     global_buffer
      - .actual_access:  write_only
        .address_space:  global
        .offset:         24
        .size:           8
        .value_kind:     global_buffer
      - .address_space:  global
        .offset:         32
        .size:           8
        .value_kind:     global_buffer
      - .address_space:  global
        .offset:         40
        .size:           8
        .value_kind:     global_buffer
      - .actual_access:  read_only
        .address_space:  global
        .offset:         48
        .size:           8
        .value_kind:     global_buffer
      - .actual_access:  read_only
        .address_space:  global
        .offset:         56
        .size:           8
        .value_kind:     global_buffer
      - .address_space:  global
        .offset:         64
        .size:           8
        .value_kind:     global_buffer
      - .address_space:  global
        .offset:         72
        .size:           8
        .value_kind:     global_buffer
      - .actual_access:  read_only
        .address_space:  global
        .offset:         80
        .size:           8
        .value_kind:     global_buffer
      - .actual_access:  read_only
        .address_space:  global
        .offset:         88
        .size:           8
        .value_kind:     global_buffer
      - .offset:         96
        .size:           4
        .value_kind:     hidden_block_count_x
      - .offset:         100
        .size:           4
        .value_kind:     hidden_block_count_y
      - .offset:         104
        .size:           4
        .value_kind:     hidden_block_count_z
      - .offset:         108
        .size:           2
        .value_kind:     hidden_group_size_x
      - .offset:         110
        .size:           2
        .value_kind:     hidden_group_size_y
      - .offset:         112
        .size:           2
        .value_kind:     hidden_group_size_z
      - .offset:         114
        .size:           2
        .value_kind:     hidden_remainder_x
      - .offset:         116
        .size:           2
        .value_kind:     hidden_remainder_y
      - .offset:         118
        .size:           2
        .value_kind:     hidden_remainder_z
      - .offset:         136
        .size:           8
        .value_kind:     hidden_global_offset_x
      - .offset:         144
        .size:           8
        .value_kind:     hidden_global_offset_y
      - .offset:         152
        .size:           8
        .value_kind:     hidden_global_offset_z
      - .offset:         160
        .size:           2
        .value_kind:     hidden_grid_dims
    .group_segment_fixed_size: 26384
    .kernarg_segment_align: 8
    .kernarg_segment_size: 352
    .language:       OpenCL C
    .language_version:
      - 2
      - 0
    .max_flat_workgroup_size: 512
    .name:           _Z12layer_kernelILb1ELi512ELi64EEvPKDv8_DF16_PKfPS0_PiS6_S6_S2_S4_S5_PfPK15HIP_vector_typeIiLj2EEPKi
    .private_segment_fixed_size: 0
    .sgpr_count:     52
    .sgpr_spill_count: 0
    .symbol:         _Z12layer_kernelILb1ELi512ELi64EEvPKDv8_DF16_PKfPS0_PiS6_S6_S2_S4_S5_PfPK15HIP_vector_typeIiLj2EEPKi.kd
    .uniform_work_group_size: 1
    .uses_dynamic_stack: false
    .vgpr_count:     61
    .vgpr_spill_count: 0
    .wavefront_size: 64
  - .agpr_count:     0
    .args:
      - .actual_access:  read_only
        .address_space:  global
        .offset:         0
        .size:           8
        .value_kind:     global_buffer
      - .actual_access:  read_only
        .address_space:  global
        .offset:         8
        .size:           8
        .value_kind:     global_buffer
      - .actual_access:  read_only
        .address_space:  global
        .offset:         16
        .size:           8
        .value_kind:     global_buffer
      - .actual_access:  read_only
        .address_space:  global
        .offset:         24
        .size:           8
        .value_kind:     global_buffer
      - .actual_access:  read_only
        .address_space:  global
        .offset:         32
        .size:           8
        .value_kind:     global_buffer
      - .actual_access:  read_only
        .address_space:  global
        .offset:         40
        .size:           8
        .value_kind:     global_buffer
      - .actual_access:  read_only
        .address_space:  global
        .offset:         48
        .size:           8
        .value_kind:     global_buffer
      - .actual_access:  read_only
        .address_space:  global
        .offset:         56
        .size:           8
        .value_kind:     global_buffer
      - .address_space:  global
        .offset:         64
        .size:           8
        .value_kind:     global_buffer
      - .address_space:  global
        .offset:         72
        .size:           8
        .value_kind:     global_buffer
      - .actual_access:  read_only
        .address_space:  global
        .offset:         80
        .size:           8
        .value_kind:     global_buffer
      - .actual_access:  read_only
        .address_space:  global
        .offset:         88
        .size:           8
        .value_kind:     global_buffer
      - .offset:         96
        .size:           4
        .value_kind:     hidden_block_count_x
      - .offset:         100
        .size:           4
        .value_kind:     hidden_block_count_y
      - .offset:         104
        .size:           4
        .value_kind:     hidden_block_count_z
      - .offset:         108
        .size:           2
        .value_kind:     hidden_group_size_x
      - .offset:         110
        .size:           2
        .value_kind:     hidden_group_size_y
      - .offset:         112
        .size:           2
        .value_kind:     hidden_group_size_z
      - .offset:         114
        .size:           2
        .value_kind:     hidden_remainder_x
      - .offset:         116
        .size:           2
        .value_kind:     hidden_remainder_y
      - .offset:         118
        .size:           2
        .value_kind:     hidden_remainder_z
      - .offset:         136
        .size:           8
        .value_kind:     hidden_global_offset_x
      - .offset:         144
        .size:           8
        .value_kind:     hidden_global_offset_y
      - .offset:         152
        .size:           8
        .value_kind:     hidden_global_offset_z
      - .offset:         160
        .size:           2
        .value_kind:     hidden_grid_dims
    .group_segment_fixed_size: 12932
    .kernarg_segment_align: 8
    .kernarg_segment_size: 352
    .language:       OpenCL C
    .language_version:
      - 2
      - 0
    .max_flat_workgroup_size: 256
    .name:           _Z12layer_kernelILb0ELi256ELi32EEvPKDv8_DF16_PKfPS0_PiS6_S6_S2_S4_S5_PfPK15HIP_vector_typeIiLj2EEPKi
    .private_segment_fixed_size: 0
    .sgpr_count:     36
    .sgpr_spill_count: 0
    .symbol:         _Z12layer_kernelILb0ELi256ELi32EEvPKDv8_DF16_PKfPS0_PiS6_S6_S2_S4_S5_PfPK15HIP_vector_typeIiLj2EEPKi.kd
    .uniform_work_group_size: 1
    .uses_dynamic_stack: false
    .vgpr_count:     64
    .vgpr_spill_count: 0
    .wavefront_size: 64
